# v35 + layer-0 XCD start stagger removed (s_sleep 20 loop -> s_nop)
# baseline (speedup 1.0000x reference)
; __global__ void __launch_bounds__(NWAVES * 64, 2) mega_fwd(Args args) {
;     ...
;         if (__builtin_amdgcn_readfirstlane((int)MISC[19])) { for (unsigned i = 0; i < (blockIdx.x & 7u); ++i) __builtin_amdgcn_s_sleep(20); }
.LBB0_423:
	s_add_i32 s26, s26, -1
	s_cmp_lg_u32 s26, 0
	s_nop 0
	s_cbranch_scc1 .LBB0_423
